# s16p + one static s_setprio 1 for waves 0-3 (other half) before the attention block loop, reset after it (L0 and L1); padded
# baseline (speedup 1.0000x reference)
; DI unsigned pk2(float lo, float hi) { const f32x2 v = {lo, hi}; return __builtin_bit_cast(unsigned, __builtin_convertvector(v, bf16x2_t)); }
; DI void attn_block(const Params& P, const Frame& F, int L, int b, int h, int qb, float lam, float oml) {
;     ...
;     const int lane = F.lane, c = lane & 15, rq = lane >> 4, wave = F.wave;
;     const int q0 = qb * 128, qrow = q0 + 16 * wave + c;
;     const size_t rowbase = (size_t)b * SEQ;
;     bf16x8 qf[2][2];
; #pragma unroll
;     for (int j = 0; j < 2; ++j)
; #pragma unroll
;         for (int ks = 0; ks < 2; ++ks) qf[j][ks] = *(const bf16x8*)(Z + (rowbase + qrow) * NZ + 3072 + h * 128 + j * 64 + 32 * ks + 8 * rq);
;     const float LOG2E = 1.4426950408889634f;
;     const float sc = 0.125f * LOG2E, sl = __builtin_bit_cast(float, __builtin_amdgcn_readfirstlane(__builtin_bit_cast(int, exp2f(-(float)(h + 1)) * LOG2E)));
; #pragma unroll
;     for (int j = 0; j < 2; ++j)
; #pragma unroll
;         for (int ks = 0; ks < 2; ++ks) { const u32x4 qv = __builtin_bit_cast(u32x4, qf[j][ks]); u32x4 o;
;             o.x = pk2(bflo(qv.x) * sc, bfhi(qv.x) * sc); o.y = pk2(bflo(qv.y) * sc, bfhi(qv.y) * sc); o.z = pk2(bflo(qv.z) * sc, bfhi(qv.z) * sc); o.w = pk2(bflo(qv.w) * sc, bfhi(qv.w) * sc);
;             qf[j][ks] = __builtin_bit_cast(bf16x8, o); }
;     float sbias[16];
; #pragma unroll
;     for (int i = 0; i < 16; ++i) sbias[i] = __builtin_bit_cast(float, __builtin_amdgcn_readfirstlane(__builtin_bit_cast(int, sl * (float)(16 * (i >> 2) + (i & 3)))));
; template <int L> DI void layer_phases(const Params& P, Frame& F, const XcdBarrier& bar, int lo, int hi) {
;     ...
;             const float li = (L == 0) ? 0.2f : 0.35550906759f;
;             const float d1 = wave_sum(P.in[I_LQ1][L * 64 + F.lane] * P.in[I_LK1][L * 64 + F.lane]), d2 = wave_sum(P.in[I_LQ2][L * 64 + F.lane] * P.in[I_LK2][L * 64 + F.lane]);
;             const float lam = __expf(d1) - __expf(d2) + li;
;             unsigned* qctr = (unsigned*)(ws + WS_CTL) + CW_QUEUE + 64 * L;
;             for (;;) {
;                 __syncthreads();
;                 if (F.tid == 0) F.MISC[24] = __hip_atomic_fetch_add(qctr, 1u, __ATOMIC_RELAXED, __HIP_MEMORY_SCOPE_AGENT);
;                 __syncthreads();
;                 const int u = (int)F.MISC[24];
;                 if (u >= 1024) break;
.LBB0_1045:
	v_ashrrev_i32_e32 v137, 31, v136
	s_waitcnt lgkmcnt(0)
	v_readlane_b32 s4, v254, 5
	v_lshlrev_b64 v[0:1], 2, v[136:137]
	v_readlane_b32 s6, v254, 7
	v_readlane_b32 s7, v254, 8
	v_readlane_b32 s8, v254, 9
	v_readlane_b32 s9, v254, 10
	v_lshl_add_u64 v[2:3], s[6:7], 0, v[0:1]
	v_readlane_b32 s10, v254, 11
	v_readlane_b32 s11, v254, 12
	v_readlane_b32 s12, v254, 13
	v_readlane_b32 s13, v254, 14
	global_load_dword v4, v[2:3], off
	v_lshl_add_u64 v[2:3], s[8:9], 0, v[0:1]
	global_load_dword v5, v[2:3], off
	v_lshl_add_u64 v[2:3], s[10:11], 0, v[0:1]
	v_lshl_add_u64 v[0:1], s[12:13], 0, v[0:1]
	global_load_dword v2, v[2:3], off
	v_xor_b32_e32 v3, 32, v193
	global_load_dword v1, v[0:1], off
	v_and_b32_e32 v0, 64, v193
	v_add_u32_e32 v12, 64, v0
	v_ashrrev_i32_e32 v6, 4, v136
	v_cmp_lt_i32_e32 vcc, v3, v12
	v_add_u32_e32 v8, 0x200, v138
	v_bfe_u32 v9, v136, 3, 1
	s_movk_i32 s6, 0x2400
	v_bfe_u32 v11, v136, 2, 2
	v_lshlrev_b32_e32 v130, 2, v6
	v_cndmask_b32_e32 v3, v193, v3, vcc
	v_ashrrev_i32_e32 v128, 4, v8
	v_mul_u32_u24_e32 v182, 0x2400, v9
	v_mad_u32_u24 v8, v9, s6, 0
	v_or_b32_e32 v9, v130, v11
	v_lshlrev_b32_e32 v190, 2, v3
	v_lshlrev_b32_e32 v7, 3, v136
	v_ashrrev_i32_e32 v114, 4, v138
	s_movk_i32 s7, 0x90
	s_movk_i32 s8, 0x110
	v_and_b32_e32 v0, 24, v7
	v_mul_lo_u32 v183, v114, s7
	v_mul_lo_u32 v188, v128, s7
	s_add_u32 s0, s54, 0x2000
	s_addc_u32 s1, s55, 0
	v_lshlrev_b32_e32 v10, 4, v136
	s_add_u32 s58, s54, 0x41600000
	v_and_b32_e32 v127, 15, v136
	v_lshlrev_b32_e32 v124, 3, v6
	v_and_b32_e32 v184, 0x70, v10
	v_add_u32_e32 v6, v8, v183
	s_addc_u32 s59, s55, 0
	s_lshl_b32 s64, s86, 4
	v_mul_lo_u32 v185, v114, s8
	v_mul_lo_u32 v189, v128, s8
	v_sub_u32_e32 v10, v130, v127
	v_readlane_b32 s5, v254, 6
	v_readlane_b32 s14, v254, 15
	v_readlane_b32 s15, v254, 16
	v_and_b32_e32 v126, 0x78, v7
	v_lshlrev_b32_e32 v186, 4, v127
	v_add_u32_e32 v7, 0, v185
	v_ashrrev_i32_e32 v131, 31, v130
	s_mov_b32 s39, 0
	v_cmp_eq_u32_e64 s[4:5], 0, v138
	v_mov_b32_e32 v113, 0
	v_and_b32_e32 v161, -16, v136
	s_movk_i32 s3, 0x3800
	s_mov_b32 s56, 0x3e38aa3b
	s_movk_i32 s33, 0x2000
	s_mov_b32 s57, 0xff800000
	v_mov_b32_e32 v179, 0x358637bd
	v_mov_b32_e32 v180, 0x42800000
	v_mov_b32_e32 v181, 0x3fb8aa3b
	v_mov_b32_e32 v116, 2.0
	v_mov_b32_e32 v117, 0x40400000
	v_mov_b32_e32 v118, 0x41800000
	v_mov_b32_e32 v119, 0x41880000
	v_mov_b32_e32 v120, 0x41900000
	v_mov_b32_e32 v121, 0x41980000
	v_mov_b32_e32 v122, 0x42000000
	v_mov_b32_e32 v123, 0x42040000
	v_ashrrev_i32_e32 v115, 31, v114
	v_mul_u32_u24_e32 v187, 0x90, v127
	v_ashrrev_i32_e32 v125, 31, v124
	v_ashrrev_i32_e32 v129, 31, v128
	v_lshl_add_u64 v[134:135], v[130:131], 2, s[14:15]
	s_add_i32 s65, 0, 0x22060
	v_add_u32_e32 v191, v7, v186
	v_mov_b32_e32 v136, 0x42080000
	v_mov_b32_e32 v137, 0x420c0000
	v_mov_b32_e32 v138, 0x42400000
	v_mov_b32_e32 v139, 0x42440000
	v_mov_b32_e32 v140, 0x42480000
	v_mov_b32_e32 v141, 0x424c0000
	s_waitcnt vmcnt(2)
	v_mul_f32_e32 v3, v4, v5
	v_mov_b32_e32 v198, 0xff800000
	v_readlane_b32 s16, v254, 17
	v_mov_b32_dpp v3, v3 quad_perm:[1,0,3,2] row_mask:0xf bank_mask:0xf bound_ctrl:1
	v_fmac_f32_e32 v3, v4, v5
	s_waitcnt vmcnt(0)
	v_mul_f32_e32 v11, v2, v1
	v_add_u32_e32 v5, v8, v188
	v_add_u32_e32 v8, 0, v189
	v_mov_b32_dpp v11, v11 quad_perm:[1,0,3,2] row_mask:0xf bank_mask:0xf bound_ctrl:1
	v_fmac_f32_e32 v11, v2, v1
	v_add_f32_dpp v1, v3, v3 quad_perm:[2,3,0,1] row_mask:0xf bank_mask:0xf bound_ctrl:1
	ds_swizzle_b32 v3, v1 offset:swizzle(SWAP,4)
	v_add_f32_dpp v2, v11, v11 quad_perm:[2,3,0,1] row_mask:0xf bank_mask:0xf bound_ctrl:1
	ds_swizzle_b32 v4, v2 offset:swizzle(SWAP,4)
	v_add_u32_e32 v193, v5, v184
	v_add_u32_e32 v194, v8, v186
	s_waitcnt lgkmcnt(1)
	v_add_f32_e32 v1, v1, v3
	ds_swizzle_b32 v3, v1 offset:swizzle(SWAP,8)
	s_waitcnt lgkmcnt(1)
	v_add_f32_e32 v2, v2, v4
	ds_swizzle_b32 v4, v2 offset:swizzle(SWAP,8)
	v_mad_u64_u32 v[132:133], s[6:7], v9, s8, v[0:1]
	s_waitcnt lgkmcnt(1)
	v_add_f32_e32 v0, v1, v3
	v_add_u32_e32 v133, v6, v184
	s_waitcnt lgkmcnt(0)
	v_add_f32_e32 v1, v2, v4
	ds_swizzle_b32 v2, v0 offset:swizzle(SWAP,16)
	ds_swizzle_b32 v3, v1 offset:swizzle(SWAP,16)
	v_or_b32_e32 v6, s64, v127
	v_subrev_u32_e32 v4, s64, v10
	v_add_u32_e32 v195, 64, v4
	s_waitcnt lgkmcnt(1)
	v_add_f32_e32 v0, v0, v2
	s_waitcnt lgkmcnt(0)
	v_add_f32_e32 v1, v1, v3
	ds_bpermute_b32 v2, v190, v0
	ds_bpermute_b32 v3, v190, v1
	v_readlane_b32 s17, v254, 18
	v_readlane_b32 s18, v254, 19
	v_readlane_b32 s19, v254, 20
	s_waitcnt lgkmcnt(1)
	v_add_f32_e32 v0, v0, v2
	s_waitcnt lgkmcnt(0)
	v_add_f32_e32 v1, v1, v3
	v_mul_f32_e32 v0, 0x3fb8aa3b, v0
	v_mul_f32_e32 v1, 0x3fb8aa3b, v1
	v_exp_f32_e32 v0, v0
	v_exp_f32_e32 v1, v1
	v_sub_u32_e32 v2, v6, v130
	v_subrev_u32_e32 v196, 64, v2
	v_sub_f32_e32 v0, v0, v1
	v_add_f32_e32 v197, 0x3e4ccccd, v0
	s_mov_b64 s[6:7], exec
	s_and_b64 exec, exec, s[4:5]
	v_mov_b32_e32 v252, 1
	global_atomic_add v252, v113, v252, s[0:1] sc0
	s_mov_b64 exec, s[6:7]
	s_cmp_lt_u32 s86, 4
	s_cbranch_scc0 .Lprio_a_done
	s_setprio 1

; DI unsigned pk2(float lo, float hi) { const f32x2 v = {lo, hi}; return __builtin_bit_cast(unsigned, __builtin_convertvector(v, bf16x2_t)); }
; DI void attn_block(const Params& P, const Frame& F, int L, int b, int h, int qb, float lam, float oml) {
;     ...
;     const int lane = F.lane, c = lane & 15, rq = lane >> 4, wave = F.wave;
;     const int q0 = qb * 128, qrow = q0 + 16 * wave + c;
;     const size_t rowbase = (size_t)b * SEQ;
;     bf16x8 qf[2][2];
; #pragma unroll
;     for (int j = 0; j < 2; ++j)
; #pragma unroll
;         for (int ks = 0; ks < 2; ++ks) qf[j][ks] = *(const bf16x8*)(Z + (rowbase + qrow) * NZ + 3072 + h * 128 + j * 64 + 32 * ks + 8 * rq);
;     const float LOG2E = 1.4426950408889634f;
;     const float sc = 0.125f * LOG2E, sl = __builtin_bit_cast(float, __builtin_amdgcn_readfirstlane(__builtin_bit_cast(int, exp2f(-(float)(h + 1)) * LOG2E)));
; #pragma unroll
;     for (int j = 0; j < 2; ++j)
; #pragma unroll
;         for (int ks = 0; ks < 2; ++ks) { const u32x4 qv = __builtin_bit_cast(u32x4, qf[j][ks]); u32x4 o;
;             o.x = pk2(bflo(qv.x) * sc, bfhi(qv.x) * sc); o.y = pk2(bflo(qv.y) * sc, bfhi(qv.y) * sc); o.z = pk2(bflo(qv.z) * sc, bfhi(qv.z) * sc); o.w = pk2(bflo(qv.w) * sc, bfhi(qv.w) * sc);
;             qf[j][ks] = __builtin_bit_cast(bf16x8, o); }
;     float sbias[16];
; #pragma unroll
;     for (int i = 0; i < 16; ++i) sbias[i] = __builtin_bit_cast(float, __builtin_amdgcn_readfirstlane(__builtin_bit_cast(int, sl * (float)(16 * (i >> 2) + (i & 3)))));
; template <int L> DI void layer_phases(const Params& P, Frame& F, const XcdBarrier& bar, int lo, int hi) {
;     ...
;             const float li = (L == 0) ? 0.2f : 0.35550906759f;
;             const float d1 = wave_sum(P.in[I_LQ1][L * 64 + F.lane] * P.in[I_LK1][L * 64 + F.lane]), d2 = wave_sum(P.in[I_LQ2][L * 64 + F.lane] * P.in[I_LK2][L * 64 + F.lane]);
;             const float lam = __expf(d1) - __expf(d2) + li;
;             unsigned* qctr = (unsigned*)(ws + WS_CTL) + CW_QUEUE + 64 * L;
;             for (;;) {
;                 __syncthreads();
;                 if (F.tid == 0) F.MISC[24] = __hip_atomic_fetch_add(qctr, 1u, __ATOMIC_RELAXED, __HIP_MEMORY_SCOPE_AGENT);
;                 __syncthreads();
;                 const int u = (int)F.MISC[24];
;                 if (u >= 1024) break;
.LBB0_2610:
	v_ashrrev_i32_e32 v113, 31, v112
	v_readlane_b32 s4, v254, 5
	v_lshlrev_b64 v[0:1], 2, v[112:113]
	v_readlane_b32 s6, v254, 7
	v_readlane_b32 s7, v254, 8
	v_readlane_b32 s8, v254, 9
	v_readlane_b32 s9, v254, 10
	v_lshl_add_u64 v[2:3], s[6:7], 0, v[0:1]
	v_readlane_b32 s10, v254, 11
	v_readlane_b32 s11, v254, 12
	v_readlane_b32 s12, v254, 13
	v_readlane_b32 s13, v254, 14
	global_load_dword v4, v[2:3], off offset:256
	v_lshl_add_u64 v[2:3], s[8:9], 0, v[0:1]
	global_load_dword v5, v[2:3], off offset:256
	v_lshl_add_u64 v[2:3], s[10:11], 0, v[0:1]
	v_lshl_add_u64 v[0:1], s[12:13], 0, v[0:1]
	global_load_dword v2, v[2:3], off offset:256
	v_xor_b32_e32 v3, 32, v154
	global_load_dword v1, v[0:1], off offset:256
	v_and_b32_e32 v0, 64, v154
	v_add_u32_e32 v12, 64, v0
	v_ashrrev_i32_e32 v6, 4, v112
	v_cmp_lt_i32_e32 vcc, v3, v12
	v_add_u32_e32 v8, 0x200, v114
	v_bfe_u32 v9, v112, 3, 1
	s_movk_i32 s6, 0x2400
	v_bfe_u32 v11, v112, 2, 2
	v_lshlrev_b32_e32 v106, 2, v6
	v_cndmask_b32_e32 v3, v154, v3, vcc
	v_ashrrev_i32_e32 v104, 4, v8
	v_mul_u32_u24_e32 v182, 0x2400, v9
	v_mad_u32_u24 v8, v9, s6, 0
	v_or_b32_e32 v9, v106, v11
	v_lshlrev_b32_e32 v190, 2, v3
	v_lshlrev_b32_e32 v7, 3, v112
	v_ashrrev_i32_e32 v98, 4, v114
	s_movk_i32 s7, 0x90
	s_movk_i32 s8, 0x110
	v_and_b32_e32 v0, 24, v7
	v_mul_lo_u32 v183, v98, s7
	v_mul_lo_u32 v188, v104, s7
	s_add_u32 s0, s54, 0x2100
	s_addc_u32 s1, s55, 0
	v_lshlrev_b32_e32 v10, 4, v112
	s_add_u32 s56, s54, 0x41600000
	v_and_b32_e32 v103, 15, v112
	v_lshlrev_b32_e32 v100, 3, v6
	v_and_b32_e32 v184, 0x70, v10
	v_add_u32_e32 v6, v8, v183
	s_addc_u32 s57, s55, 0
	s_lshl_b32 s66, s86, 4
	v_mul_lo_u32 v185, v98, s8
	v_mul_lo_u32 v189, v104, s8
	v_sub_u32_e32 v10, v106, v103
	v_readlane_b32 s5, v254, 6
	v_readlane_b32 s14, v254, 15
	v_readlane_b32 s15, v254, 16
	v_and_b32_e32 v102, 0x78, v7
	v_lshlrev_b32_e32 v186, 4, v103
	v_add_u32_e32 v7, 0, v185
	v_ashrrev_i32_e32 v107, 31, v106
	s_mov_b32 s41, 0
	v_cmp_eq_u32_e64 s[4:5], 0, v114
	v_mov_b32_e32 v97, 0
	v_and_b32_e32 v145, -16, v112
	s_movk_i32 s3, 0x3ff
	s_movk_i32 s33, 0x3800
	s_mov_b64 s[42:43], 0x1800
	s_movk_i32 s47, 0x1000
	s_mov_b32 s62, 0x42fc0000
	s_mov_b32 s46, 0x3e38aa3b
	s_movk_i32 s63, 0x2000
	s_mov_b32 s64, 0xff800000
	v_mov_b32_e32 v163, 0x358637bd
	s_mov_b64 s[48:49], 0x61400400
	s_mov_b32 s65, 0x61400000
	v_mov_b32_e32 v180, 0x42800000
	v_mov_b32_e32 v181, 0x3fb8aa3b
	v_ashrrev_i32_e32 v99, 31, v98
	v_mul_u32_u24_e32 v187, 0x90, v103
	v_ashrrev_i32_e32 v101, 31, v100
	v_ashrrev_i32_e32 v105, 31, v104
	v_lshl_add_u64 v[110:111], v[106:107], 2, s[14:15]
	s_add_i32 s67, 0, 0x22060
	v_add_u32_e32 v191, v7, v186
	v_mov_b32_e32 v112, 2.0
	v_mov_b32_e32 v113, 0x40400000
	v_mov_b32_e32 v114, 0x41800000
	v_mov_b32_e32 v115, 0x41880000
	v_mov_b32_e32 v116, 0x41900000
	v_mov_b32_e32 v117, 0x41980000
	v_mov_b32_e32 v118, 0x42000000
	v_mov_b32_e32 v119, 0x42040000
	s_waitcnt vmcnt(2)
	v_mul_f32_e32 v3, v4, v5
	v_mov_b32_e32 v120, 0x42080000
	v_mov_b32_e32 v121, 0x420c0000
	v_mov_b32_dpp v3, v3 quad_perm:[1,0,3,2] row_mask:0xf bank_mask:0xf bound_ctrl:1
	v_fmac_f32_e32 v3, v4, v5
	s_waitcnt vmcnt(0)
	v_mul_f32_e32 v11, v2, v1
	v_add_u32_e32 v5, v8, v188
	v_add_u32_e32 v8, 0, v189
	v_mov_b32_dpp v11, v11 quad_perm:[1,0,3,2] row_mask:0xf bank_mask:0xf bound_ctrl:1
	v_fmac_f32_e32 v11, v2, v1
	v_add_f32_dpp v1, v3, v3 quad_perm:[2,3,0,1] row_mask:0xf bank_mask:0xf bound_ctrl:1
	ds_swizzle_b32 v3, v1 offset:swizzle(SWAP,4)
	v_add_f32_dpp v2, v11, v11 quad_perm:[2,3,0,1] row_mask:0xf bank_mask:0xf bound_ctrl:1
	ds_swizzle_b32 v4, v2 offset:swizzle(SWAP,4)
	v_add_u32_e32 v193, v5, v184
	v_add_u32_e32 v194, v8, v186
	s_waitcnt lgkmcnt(1)
	v_add_f32_e32 v1, v1, v3
	ds_swizzle_b32 v3, v1 offset:swizzle(SWAP,8)
	s_waitcnt lgkmcnt(1)
	v_add_f32_e32 v2, v2, v4
	ds_swizzle_b32 v4, v2 offset:swizzle(SWAP,8)
	v_mad_u64_u32 v[108:109], s[6:7], v9, s8, v[0:1]
	s_waitcnt lgkmcnt(1)
	v_add_f32_e32 v0, v1, v3
	v_add_u32_e32 v109, v6, v184
	s_waitcnt lgkmcnt(0)
	v_add_f32_e32 v1, v2, v4
	ds_swizzle_b32 v2, v0 offset:swizzle(SWAP,16)
	ds_swizzle_b32 v3, v1 offset:swizzle(SWAP,16)
	v_or_b32_e32 v6, s66, v103
	v_subrev_u32_e32 v4, s66, v10
	v_add_u32_e32 v195, 64, v4
	s_waitcnt lgkmcnt(1)
	v_add_f32_e32 v0, v0, v2
	s_waitcnt lgkmcnt(0)
	v_add_f32_e32 v1, v1, v3
	ds_bpermute_b32 v2, v190, v0
	ds_bpermute_b32 v3, v190, v1
	v_mov_b32_e32 v122, 0x42400000
	v_mov_b32_e32 v123, 0x42440000
	v_mov_b32_e32 v124, 0x42480000
	s_waitcnt lgkmcnt(1)
	v_add_f32_e32 v0, v0, v2
	s_waitcnt lgkmcnt(0)
	v_add_f32_e32 v1, v1, v3
	v_mul_f32_e32 v0, 0x3fb8aa3b, v0
	v_mul_f32_e32 v1, 0x3fb8aa3b, v1
	v_exp_f32_e32 v0, v0
	v_exp_f32_e32 v1, v1
	v_sub_u32_e32 v2, v6, v106
	v_subrev_u32_e32 v196, 64, v2
	v_mov_b32_e32 v125, 0x424c0000
	v_sub_f32_e32 v0, v0, v1
	v_add_f32_e32 v197, 0x3eb60549, v0
	v_mov_b32_e32 v198, 0xff800000
	v_readlane_b32 s16, v254, 17
	v_readlane_b32 s17, v254, 18
	v_readlane_b32 s18, v254, 19
	v_readlane_b32 s19, v254, 20
	s_mov_b64 s[6:7], exec
	s_and_b64 exec, exec, s[4:5]
	v_mov_b32_e32 v252, 1
	global_atomic_add v252, v97, v252, s[0:1] sc0
	s_mov_b64 exec, s[6:7]
	s_cmp_lt_u32 s86, 4
	s_cbranch_scc0 .Lprio_b_done
	s_setprio 1
